# MLA up-projection GEMM: column-block assignment of waves 4-7 rotated by two (wc ^= wr<<1) so that each SIMD hosts one rope-column wave and one plain wave in the epilogue
# baseline (speedup 1.0000x reference)
.LBB0_388:
	s_add_u32 s77, s18, 0x200000
	s_addc_u32 s78, s19, 0
	s_add_u32 s38, s18, 0x180000
	s_addc_u32 s39, s19, 0
	s_add_u32 s40, s18, 0x33980000
	s_addc_u32 s41, s19, 0
	s_add_i32 s79, s66, 0x18000
	s_or_b32 s7, s10, 0x80
	s_mov_b32 s26, s22
	s_mov_b32 s27, s23
	s_mov_b32 m0, s79
	s_add_i32 s80, s66, 0x1a000
	s_waitcnt vmcnt(2)
	s_barrier
	buffer_load_dwordx4 v200, s[24:27], s7 offen lds
	s_mov_b32 m0, s80
	s_add_i32 s81, s66, 0x8000
	buffer_load_dwordx4 v204, s[24:27], s7 offen lds
	s_or_b32 s7, s11, 0x80
	s_mov_b32 m0, s81
	s_add_i32 s82, s66, 0xa000
	buffer_load_dwordx4 v198, s[20:23], s7 offen lds
	s_mov_b32 m0, s82
	s_add_i32 s83, s66, 0x1c000
	buffer_load_dwordx4 v202, s[20:23], s7 offen lds
	s_or_b32 s7, s10, 0x20080
	s_mov_b32 m0, s83
	s_add_i32 s84, s66, 0x1e000
	buffer_load_dwordx4 v200, s[24:27], s7 offen lds
	s_mov_b32 m0, s84
	s_lshl_b32 s85, s5, 6
	buffer_load_dwordx4 v204, s[24:27], s7 offen lds
	s_and_b32 s7, s4, 3
	s_lshl_b32 s4, s5, 1
	s_xor_b32 s7, s7, s4
	v_and_b32_e32 v1, 48, v0
	s_lshl_b32 s4, s5, 13
	v_lshlrev_b32_e32 v2, 6, v0
	s_movk_i32 s5, 0x3c0
	v_lshlrev_b32_e32 v0, 2, v0
	v_and_or_b32 v1, v2, s5, v1
	v_and_b32_e32 v0, 32, v0
	v_bitop3_b32 v2, v1, s4, v0 bitop3:0xde
	s_lshl_b32 s86, s7, 5
	s_lshl_b32 s4, s7, 12
	s_add_i32 s87, s66, 0xc000
	s_cmpk_lt_u32 s9, 0x100
	s_cselect_b64 s[42:43], -1, 0
	s_cmp_lt_u32 s7, 2
	v_bitop3_b32 v0, s4, v1, v0 bitop3:0xf6
	s_cselect_b64 s[44:45], -1, 0
	s_lshl_b32 s4, s7, 2
	s_add_i32 s88, s4, 0
	s_add_i32 s88, s88, 0x20000
	s_cmp_eq_u32 s7, 0
	s_waitcnt vmcnt(6)
	s_cselect_b64 s[4:5], -1, 0
	s_add_i32 s89, s66, 0xe000
	s_lshl_b32 s7, s7, 6
	v_add_u32_e32 v0, 0, v0
	s_add_u32 s50, s20, s7
	v_add_u32_e32 v199, 0x10000, v0
	v_add_u32_e32 v201, 0x14000, v0
	v_add_u32_e32 v205, 0x18000, v0
	v_add_u32_e32 v211, 0x1c000, v0
	v_mbcnt_lo_u32_b32 v0, -1, 0
	s_addc_u32 s51, s6, 0
	v_add_u32_e32 v203, 0, v2
	v_mov_b32_e32 v213, 0x358637bd
	s_mov_b32 s90, 0xf800000
	v_mov_b32_e32 v215, 0x260
	v_mbcnt_hi_u32_b32 v221, -1, v0
	v_mov_b32_e32 v207, 0
	s_movk_i32 s91, 0xc00
	s_lshl_b32 s34, s86, 1
	s_mov_b32 s92, s35
	s_barrier
	s_branch .LBB0_391
